# stack12 + grid-barrier poll loops back off s_sleep 6 between polls (back-off tuning between 4 and 10)
# baseline (speedup 1.0000x reference)
.LBB0_101:
	global_load_dword v16, v17, s[6:7] sc1
	global_load_dword v1, v17, s[8:9] sc1
	global_load_dword v2, v17, s[10:11] sc1
	global_load_dword v3, v17, s[12:13] sc1
	global_load_dword v4, v17, s[14:15] sc1
	global_load_dword v5, v17, s[16:17] sc1
	global_load_dword v6, v17, s[18:19] sc1
	global_load_dword v7, v17, s[20:21] sc1
	global_load_dword v8, v17, s[22:23] sc1
	global_load_dword v9, v17, s[24:25] sc1
	global_load_dword v10, v17, s[26:27] sc1
	global_load_dword v11, v17, s[28:29] sc1
	global_load_dword v12, v17, s[30:31] sc1
	global_load_dword v13, v17, s[34:35] sc1
	global_load_dword v14, v17, s[36:37] sc1
	global_load_dword v15, v17, s[38:39] sc1
	s_mov_b64 s[40:41], -1
	s_mov_b64 s[42:43], -1
	s_waitcnt vmcnt(14)
	v_add_u32_e32 v18, v1, v16
	s_waitcnt vmcnt(13)
	v_add_u32_e32 v18, v18, v2
	s_waitcnt vmcnt(12)
	v_add_u32_e32 v18, v18, v3
	s_waitcnt vmcnt(11)
	v_add_u32_e32 v18, v18, v4
	s_waitcnt vmcnt(10)
	v_add_u32_e32 v18, v18, v5
	s_waitcnt vmcnt(9)
	v_add_u32_e32 v18, v18, v6
	s_waitcnt vmcnt(8)
	v_add_u32_e32 v18, v18, v7
	s_waitcnt vmcnt(7)
	v_add_u32_e32 v18, v18, v8
	s_waitcnt vmcnt(6)
	v_add_u32_e32 v18, v18, v9
	s_waitcnt vmcnt(5)
	v_add_u32_e32 v18, v18, v10
	s_waitcnt vmcnt(4)
	v_add_u32_e32 v18, v18, v11
	s_waitcnt vmcnt(3)
	v_add_u32_e32 v18, v18, v12
	s_waitcnt vmcnt(2)
	v_add_u32_e32 v18, v18, v13
	s_waitcnt vmcnt(1)
	v_add_u32_e32 v18, v18, v14
	s_waitcnt vmcnt(0)
	v_add_u32_e32 v18, v18, v15
	v_cmp_eq_u32_e32 vcc, s33, v18
	s_cbranch_vccnz .LBB0_100
	s_and_b32 s40, s47, 0xff
	s_cmp_eq_u32 s40, 0
	s_mov_b64 s[40:41], -1
	s_mov_b64 s[44:45], -1
	s_sleep 6
	s_cbranch_scc0 .LBB0_105
	global_load_dword v18, v17, s[4:5] sc1
	s_waitcnt vmcnt(0)
	v_cmp_eq_u32_e32 vcc, 0, v18
	s_cbranch_vccnz .LBB0_107
	s_mov_b64 s[44:45], 0

.LBB0_119:
	s_and_b32 s20, s24, 0xff
	s_mov_b64 s[18:19], -1
	s_cmp_lg_u32 s20, 0
	s_mov_b64 s[22:23], -1
	s_sleep 6
	s_cbranch_scc1 .LBB0_122
	global_load_dword v3, v1, s[10:11] sc1
	s_waitcnt vmcnt(0)
	v_cmp_eq_u32_e32 vcc, 0, v3
	s_cbranch_vccnz .LBB0_124
	s_mov_b64 s[22:23], 0
	s_mov_b64 s[20:21], -1

.LBB0_136:
	s_and_b32 s18, s24, 0xff
	s_cmp_lg_u32 s18, 0
	s_mov_b64 s[20:21], -1
	s_sleep 6
	s_cbranch_scc1 .LBB0_139
	global_load_dword v2, v1, s[10:11] sc1
	s_waitcnt vmcnt(0)
	v_cmp_eq_u32_e32 vcc, 0, v2
	s_cbranch_vccnz .LBB0_141
	s_mov_b64 s[20:21], 0
	s_mov_b64 s[18:19], -1

.LBB0_533:
	global_load_dword v16, v17, s[6:7] sc1
	global_load_dword v1, v17, s[8:9] sc1
	global_load_dword v2, v17, s[10:11] sc1
	global_load_dword v3, v17, s[12:13] sc1
	global_load_dword v4, v17, s[14:15] sc1
	global_load_dword v5, v17, s[16:17] sc1
	global_load_dword v6, v17, s[18:19] sc1
	global_load_dword v7, v17, s[20:21] sc1
	global_load_dword v8, v17, s[22:23] sc1
	global_load_dword v9, v17, s[24:25] sc1
	global_load_dword v10, v17, s[26:27] sc1
	global_load_dword v11, v17, s[28:29] sc1
	global_load_dword v12, v17, s[30:31] sc1
	global_load_dword v13, v17, s[34:35] sc1
	global_load_dword v14, v17, s[36:37] sc1
	global_load_dword v15, v17, s[38:39] sc1
	s_mov_b64 s[40:41], -1
	s_mov_b64 s[42:43], -1
	s_waitcnt vmcnt(14)
	v_add_u32_e32 v18, v1, v16
	s_waitcnt vmcnt(13)
	v_add_u32_e32 v18, v18, v2
	s_waitcnt vmcnt(12)
	v_add_u32_e32 v18, v18, v3
	s_waitcnt vmcnt(11)
	v_add_u32_e32 v18, v18, v4
	s_waitcnt vmcnt(10)
	v_add_u32_e32 v18, v18, v5
	s_waitcnt vmcnt(9)
	v_add_u32_e32 v18, v18, v6
	s_waitcnt vmcnt(8)
	v_add_u32_e32 v18, v18, v7
	s_waitcnt vmcnt(7)
	v_add_u32_e32 v18, v18, v8
	s_waitcnt vmcnt(6)
	v_add_u32_e32 v18, v18, v9
	s_waitcnt vmcnt(5)
	v_add_u32_e32 v18, v18, v10
	s_waitcnt vmcnt(4)
	v_add_u32_e32 v18, v18, v11
	s_waitcnt vmcnt(3)
	v_add_u32_e32 v18, v18, v12
	s_waitcnt vmcnt(2)
	v_add_u32_e32 v18, v18, v13
	s_waitcnt vmcnt(1)
	v_add_u32_e32 v18, v18, v14
	s_waitcnt vmcnt(0)
	v_add_u32_e32 v18, v18, v15
	v_cmp_eq_u32_e32 vcc, s33, v18
	s_cbranch_vccnz .LBB0_532
	s_and_b32 s40, s46, 0xff
	s_cmp_eq_u32 s40, 0
	s_mov_b64 s[40:41], -1
	s_mov_b64 s[44:45], -1
	s_sleep 6
	s_cbranch_scc0 .LBB0_537
	global_load_dword v18, v17, s[4:5] sc1
	s_waitcnt vmcnt(0)
	v_cmp_eq_u32_e32 vcc, 0, v18
	s_cbranch_vccnz .LBB0_539
	s_mov_b64 s[44:45], 0

.LBB0_1358:
	global_load_dword v16, v17, s[8:9] sc1
	global_load_dword v1, v17, s[10:11] sc1
	global_load_dword v2, v17, s[12:13] sc1
	global_load_dword v3, v17, s[14:15] sc1
	global_load_dword v4, v17, s[16:17] sc1
	global_load_dword v5, v17, s[18:19] sc1
	global_load_dword v6, v17, s[20:21] sc1
	global_load_dword v7, v17, s[22:23] sc1
	global_load_dword v8, v17, s[24:25] sc1
	global_load_dword v9, v17, s[26:27] sc1
	global_load_dword v10, v17, s[28:29] sc1
	global_load_dword v11, v17, s[30:31] sc1
	global_load_dword v12, v17, s[34:35] sc1
	global_load_dword v13, v17, s[36:37] sc1
	global_load_dword v14, v17, s[38:39] sc1
	global_load_dword v15, v17, s[40:41] sc1
	s_mov_b64 s[42:43], -1
	s_mov_b64 s[44:45], -1
	s_waitcnt vmcnt(14)
	v_add_u32_e32 v18, v1, v16
	s_waitcnt vmcnt(13)
	v_add_u32_e32 v18, v18, v2
	s_waitcnt vmcnt(12)
	v_add_u32_e32 v18, v18, v3
	s_waitcnt vmcnt(11)
	v_add_u32_e32 v18, v18, v4
	s_waitcnt vmcnt(10)
	v_add_u32_e32 v18, v18, v5
	s_waitcnt vmcnt(9)
	v_add_u32_e32 v18, v18, v6
	s_waitcnt vmcnt(8)
	v_add_u32_e32 v18, v18, v7
	s_waitcnt vmcnt(7)
	v_add_u32_e32 v18, v18, v8
	s_waitcnt vmcnt(6)
	v_add_u32_e32 v18, v18, v9
	s_waitcnt vmcnt(5)
	v_add_u32_e32 v18, v18, v10
	s_waitcnt vmcnt(4)
	v_add_u32_e32 v18, v18, v11
	s_waitcnt vmcnt(3)
	v_add_u32_e32 v18, v18, v12
	s_waitcnt vmcnt(2)
	v_add_u32_e32 v18, v18, v13
	s_waitcnt vmcnt(1)
	v_add_u32_e32 v18, v18, v14
	s_waitcnt vmcnt(0)
	v_add_u32_e32 v18, v18, v15
	v_cmp_eq_u32_e32 vcc, s33, v18
	s_cbranch_vccnz .LBB0_1357
	s_and_b32 s42, s48, 0xff
	s_cmp_eq_u32 s42, 0
	s_mov_b64 s[42:43], -1
	s_mov_b64 s[46:47], -1
	s_sleep 6
	s_cbranch_scc0 .LBB0_1362
	global_load_dword v18, v17, s[6:7] sc1
	s_waitcnt vmcnt(0)
	v_cmp_eq_u32_e32 vcc, 0, v18
	s_cbranch_vccnz .LBB0_1364
	s_mov_b64 s[46:47], 0

.LBB0_1376:
	s_and_b32 s22, s26, 0xff
	s_mov_b64 s[20:21], -1
	s_cmp_lg_u32 s22, 0
	s_mov_b64 s[24:25], -1
	s_sleep 6
	s_cbranch_scc1 .LBB0_1379
	global_load_dword v3, v1, s[12:13] sc1
	s_waitcnt vmcnt(0)
	v_cmp_eq_u32_e32 vcc, 0, v3
	s_cbranch_vccnz .LBB0_1381
	s_mov_b64 s[24:25], 0
	s_mov_b64 s[22:23], -1

.LBB0_1393:
	s_and_b32 s20, s26, 0xff
	s_cmp_lg_u32 s20, 0
	s_mov_b64 s[22:23], -1
	s_sleep 6
	s_cbranch_scc1 .LBB0_1396
	global_load_dword v2, v1, s[12:13] sc1
	s_waitcnt vmcnt(0)
	v_cmp_eq_u32_e32 vcc, 0, v2
	s_cbranch_vccnz .LBB0_1398
	s_mov_b64 s[22:23], 0
	s_mov_b64 s[20:21], -1

.LBB0_1491:
	global_load_dword v16, v17, s[8:9] sc1
	global_load_dword v1, v17, s[10:11] sc1
	global_load_dword v2, v17, s[12:13] sc1
	global_load_dword v3, v17, s[14:15] sc1
	global_load_dword v4, v17, s[16:17] sc1
	global_load_dword v5, v17, s[18:19] sc1
	global_load_dword v6, v17, s[22:23] sc1
	global_load_dword v7, v17, s[24:25] sc1
	global_load_dword v8, v17, s[26:27] sc1
	global_load_dword v9, v17, s[28:29] sc1
	global_load_dword v10, v17, s[30:31] sc1
	global_load_dword v11, v17, s[34:35] sc1
	global_load_dword v12, v17, s[36:37] sc1
	global_load_dword v13, v17, s[38:39] sc1
	global_load_dword v14, v17, s[40:41] sc1
	global_load_dword v15, v17, s[42:43] sc1
	s_mov_b64 s[44:45], -1
	s_mov_b64 s[46:47], -1
	s_waitcnt vmcnt(14)
	v_add_u32_e32 v18, v1, v16
	s_waitcnt vmcnt(13)
	v_add_u32_e32 v18, v18, v2
	s_waitcnt vmcnt(12)
	v_add_u32_e32 v18, v18, v3
	s_waitcnt vmcnt(11)
	v_add_u32_e32 v18, v18, v4
	s_waitcnt vmcnt(10)
	v_add_u32_e32 v18, v18, v5
	s_waitcnt vmcnt(9)
	v_add_u32_e32 v18, v18, v6
	s_waitcnt vmcnt(8)
	v_add_u32_e32 v18, v18, v7
	s_waitcnt vmcnt(7)
	v_add_u32_e32 v18, v18, v8
	s_waitcnt vmcnt(6)
	v_add_u32_e32 v18, v18, v9
	s_waitcnt vmcnt(5)
	v_add_u32_e32 v18, v18, v10
	s_waitcnt vmcnt(4)
	v_add_u32_e32 v18, v18, v11
	s_waitcnt vmcnt(3)
	v_add_u32_e32 v18, v18, v12
	s_waitcnt vmcnt(2)
	v_add_u32_e32 v18, v18, v13
	s_waitcnt vmcnt(1)
	v_add_u32_e32 v18, v18, v14
	s_waitcnt vmcnt(0)
	v_add_u32_e32 v18, v18, v15
	v_cmp_eq_u32_e32 vcc, s33, v18
	s_cbranch_vccnz .LBB0_1490
	s_and_b32 s44, s50, 0xff
	s_cmp_eq_u32 s44, 0
	s_mov_b64 s[44:45], -1
	s_mov_b64 s[48:49], -1
	s_sleep 6
	s_cbranch_scc0 .LBB0_1495
	global_load_dword v18, v17, s[6:7] sc1
	s_waitcnt vmcnt(0)
	v_cmp_eq_u32_e32 vcc, 0, v18
	s_cbranch_vccnz .LBB0_1497
	s_mov_b64 s[48:49], 0

.LBB0_1509:
	s_and_b32 s24, s28, 0xff
	s_mov_b64 s[22:23], -1
	s_cmp_lg_u32 s24, 0
	s_mov_b64 s[26:27], -1
	s_sleep 6
	s_cbranch_scc1 .LBB0_1512
	global_load_dword v3, v1, s[12:13] sc1
	s_waitcnt vmcnt(0)
	v_cmp_eq_u32_e32 vcc, 0, v3
	s_cbranch_vccnz .LBB0_1514
	s_mov_b64 s[26:27], 0
	s_mov_b64 s[24:25], -1

.LBB0_1526:
	s_and_b32 s22, s28, 0xff
	s_cmp_lg_u32 s22, 0
	s_mov_b64 s[24:25], -1
	s_sleep 6
	s_cbranch_scc1 .LBB0_1529
	global_load_dword v2, v1, s[12:13] sc1
	s_waitcnt vmcnt(0)
	v_cmp_eq_u32_e32 vcc, 0, v2
	s_cbranch_vccnz .LBB0_1531
	s_mov_b64 s[24:25], 0
	s_mov_b64 s[22:23], -1

.LBB0_2204:
	global_load_dword v16, v17, s[6:7] sc1
	global_load_dword v1, v17, s[8:9] sc1
	global_load_dword v2, v17, s[10:11] sc1
	global_load_dword v3, v17, s[12:13] sc1
	global_load_dword v4, v17, s[14:15] sc1
	global_load_dword v5, v17, s[16:17] sc1
	global_load_dword v6, v17, s[18:19] sc1
	global_load_dword v7, v17, s[22:23] sc1
	global_load_dword v8, v17, s[24:25] sc1
	global_load_dword v9, v17, s[26:27] sc1
	global_load_dword v10, v17, s[28:29] sc1
	global_load_dword v11, v17, s[30:31] sc1
	global_load_dword v12, v17, s[34:35] sc1
	global_load_dword v13, v17, s[36:37] sc1
	global_load_dword v14, v17, s[38:39] sc1
	global_load_dword v15, v17, s[40:41] sc1
	s_mov_b64 s[42:43], -1
	s_mov_b64 s[44:45], -1
	s_waitcnt vmcnt(14)
	v_add_u32_e32 v18, v1, v16
	s_waitcnt vmcnt(13)
	v_add_u32_e32 v18, v18, v2
	s_waitcnt vmcnt(12)
	v_add_u32_e32 v18, v18, v3
	s_waitcnt vmcnt(11)
	v_add_u32_e32 v18, v18, v4
	s_waitcnt vmcnt(10)
	v_add_u32_e32 v18, v18, v5
	s_waitcnt vmcnt(9)
	v_add_u32_e32 v18, v18, v6
	s_waitcnt vmcnt(8)
	v_add_u32_e32 v18, v18, v7
	s_waitcnt vmcnt(7)
	v_add_u32_e32 v18, v18, v8
	s_waitcnt vmcnt(6)
	v_add_u32_e32 v18, v18, v9
	s_waitcnt vmcnt(5)
	v_add_u32_e32 v18, v18, v10
	s_waitcnt vmcnt(4)
	v_add_u32_e32 v18, v18, v11
	s_waitcnt vmcnt(3)
	v_add_u32_e32 v18, v18, v12
	s_waitcnt vmcnt(2)
	v_add_u32_e32 v18, v18, v13
	s_waitcnt vmcnt(1)
	v_add_u32_e32 v18, v18, v14
	s_waitcnt vmcnt(0)
	v_add_u32_e32 v18, v18, v15
	v_cmp_eq_u32_e32 vcc, s33, v18
	s_cbranch_vccnz .LBB0_2203
	s_and_b32 s42, s48, 0xff
	s_cmp_eq_u32 s42, 0
	s_mov_b64 s[42:43], -1
	s_mov_b64 s[46:47], -1
	s_sleep 6
	s_cbranch_scc0 .LBB0_2208
	global_load_dword v18, v17, s[4:5] sc1
	s_waitcnt vmcnt(0)
	v_cmp_eq_u32_e32 vcc, 0, v18
	s_cbranch_vccnz .LBB0_2210
	s_mov_b64 s[46:47], 0

.LBB0_2222:
	s_and_b32 s22, s26, 0xff
	s_mov_b64 s[18:19], -1
	s_cmp_lg_u32 s22, 0
	s_mov_b64 s[24:25], -1
	s_sleep 6
	s_cbranch_scc1 .LBB0_2225
	global_load_dword v3, v1, s[10:11] sc1
	s_waitcnt vmcnt(0)
	v_cmp_eq_u32_e32 vcc, 0, v3
	s_cbranch_vccnz .LBB0_2227
	s_mov_b64 s[24:25], 0
	s_mov_b64 s[22:23], -1

.LBB0_2239:
	s_and_b32 s18, s26, 0xff
	s_cmp_lg_u32 s18, 0
	s_mov_b64 s[22:23], -1
	s_sleep 6
	s_cbranch_scc1 .LBB0_2242
	global_load_dword v2, v1, s[10:11] sc1
	s_waitcnt vmcnt(0)
	v_cmp_eq_u32_e32 vcc, 0, v2
	s_cbranch_vccnz .LBB0_2244
	s_mov_b64 s[22:23], 0
	s_mov_b64 s[18:19], -1

.LBB0_2307:
	global_load_dword v16, v17, s[6:7] sc1
	global_load_dword v1, v17, s[8:9] sc1
	global_load_dword v2, v17, s[10:11] sc1
	global_load_dword v3, v17, s[12:13] sc1
	global_load_dword v4, v17, s[16:17] sc1
	global_load_dword v5, v17, s[18:19] sc1
	global_load_dword v6, v17, s[22:23] sc1
	global_load_dword v7, v17, s[24:25] sc1
	global_load_dword v8, v17, s[26:27] sc1
	global_load_dword v9, v17, s[28:29] sc1
	global_load_dword v10, v17, s[30:31] sc1
	global_load_dword v11, v17, s[34:35] sc1
	global_load_dword v12, v17, s[36:37] sc1
	global_load_dword v13, v17, s[38:39] sc1
	global_load_dword v14, v17, s[40:41] sc1
	global_load_dword v15, v17, s[42:43] sc1
	s_mov_b64 s[44:45], -1
	s_mov_b64 s[46:47], -1
	s_waitcnt vmcnt(14)
	v_add_u32_e32 v18, v1, v16
	s_waitcnt vmcnt(13)
	v_add_u32_e32 v18, v18, v2
	s_waitcnt vmcnt(12)
	v_add_u32_e32 v18, v18, v3
	s_waitcnt vmcnt(11)
	v_add_u32_e32 v18, v18, v4
	s_waitcnt vmcnt(10)
	v_add_u32_e32 v18, v18, v5
	s_waitcnt vmcnt(9)
	v_add_u32_e32 v18, v18, v6
	s_waitcnt vmcnt(8)
	v_add_u32_e32 v18, v18, v7
	s_waitcnt vmcnt(7)
	v_add_u32_e32 v18, v18, v8
	s_waitcnt vmcnt(6)
	v_add_u32_e32 v18, v18, v9
	s_waitcnt vmcnt(5)
	v_add_u32_e32 v18, v18, v10
	s_waitcnt vmcnt(4)
	v_add_u32_e32 v18, v18, v11
	s_waitcnt vmcnt(3)
	v_add_u32_e32 v18, v18, v12
	s_waitcnt vmcnt(2)
	v_add_u32_e32 v18, v18, v13
	s_waitcnt vmcnt(1)
	v_add_u32_e32 v18, v18, v14
	s_waitcnt vmcnt(0)
	v_add_u32_e32 v18, v18, v15
	v_cmp_eq_u32_e32 vcc, s51, v18
	s_cbranch_vccnz .LBB0_2306
	s_and_b32 s44, s58, 0xff
	s_cmp_eq_u32 s44, 0
	s_mov_b64 s[44:45], -1
	s_mov_b64 s[48:49], -1
	s_sleep 6
	s_cbranch_scc0 .LBB0_2311
	global_load_dword v18, v17, s[4:5] sc1
	s_waitcnt vmcnt(0)
	v_cmp_eq_u32_e32 vcc, 0, v18
	s_cbranch_vccnz .LBB0_2313
	s_mov_b64 s[48:49], 0

.LBB0_2325:
	s_and_b32 s24, s28, 0xff
	s_mov_b64 s[22:23], -1
	s_cmp_lg_u32 s24, 0
	s_mov_b64 s[26:27], -1
	s_sleep 6
	s_cbranch_scc1 .LBB0_2328
	global_load_dword v3, v1, s[10:11] sc1
	s_waitcnt vmcnt(0)
	v_cmp_eq_u32_e32 vcc, 0, v3
	s_cbranch_vccnz .LBB0_2330
	s_mov_b64 s[26:27], 0
	s_mov_b64 s[24:25], -1

.LBB0_2342:
	s_and_b32 s22, s28, 0xff
	s_cmp_lg_u32 s22, 0
	s_mov_b64 s[24:25], -1
	s_sleep 6
	s_cbranch_scc1 .LBB0_2345
	global_load_dword v2, v1, s[10:11] sc1
	s_waitcnt vmcnt(0)
	v_cmp_eq_u32_e32 vcc, 0, v2
	s_cbranch_vccnz .LBB0_2347
	s_mov_b64 s[24:25], 0
	s_mov_b64 s[22:23], -1

.LBB0_2378:
	global_load_dword v16, v17, s[8:9] sc1
	global_load_dword v1, v17, s[10:11] sc1
	global_load_dword v2, v17, s[12:13] sc1
	global_load_dword v3, v17, s[16:17] sc1
	global_load_dword v4, v17, s[18:19] sc1
	global_load_dword v5, v17, s[22:23] sc1
	global_load_dword v6, v17, s[24:25] sc1
	global_load_dword v7, v17, s[26:27] sc1
	global_load_dword v8, v17, s[28:29] sc1
	global_load_dword v9, v17, s[30:31] sc1
	global_load_dword v10, v17, s[34:35] sc1
	global_load_dword v11, v17, s[36:37] sc1
	global_load_dword v12, v17, s[38:39] sc1
	global_load_dword v13, v17, s[40:41] sc1
	global_load_dword v14, v17, s[42:43] sc1
	global_load_dword v15, v17, s[44:45] sc1
	s_mov_b64 s[46:47], -1
	s_mov_b64 s[48:49], -1
	s_waitcnt vmcnt(14)
	v_add_u32_e32 v18, v1, v16
	s_waitcnt vmcnt(13)
	v_add_u32_e32 v18, v18, v2
	s_waitcnt vmcnt(12)
	v_add_u32_e32 v18, v18, v3
	s_waitcnt vmcnt(11)
	v_add_u32_e32 v18, v18, v4
	s_waitcnt vmcnt(10)
	v_add_u32_e32 v18, v18, v5
	s_waitcnt vmcnt(9)
	v_add_u32_e32 v18, v18, v6
	s_waitcnt vmcnt(8)
	v_add_u32_e32 v18, v18, v7
	s_waitcnt vmcnt(7)
	v_add_u32_e32 v18, v18, v8
	s_waitcnt vmcnt(6)
	v_add_u32_e32 v18, v18, v9
	s_waitcnt vmcnt(5)
	v_add_u32_e32 v18, v18, v10
	s_waitcnt vmcnt(4)
	v_add_u32_e32 v18, v18, v11
	s_waitcnt vmcnt(3)
	v_add_u32_e32 v18, v18, v12
	s_waitcnt vmcnt(2)
	v_add_u32_e32 v18, v18, v13
	s_waitcnt vmcnt(1)
	v_add_u32_e32 v18, v18, v14
	s_waitcnt vmcnt(0)
	v_add_u32_e32 v18, v18, v15
	v_cmp_eq_u32_e32 vcc, s59, v18
	s_cbranch_vccnz .LBB0_2377
	s_and_b32 s46, s60, 0xff
	s_cmp_eq_u32 s46, 0
	s_mov_b64 s[46:47], -1
	s_mov_b64 s[50:51], -1
	s_sleep 6
	s_cbranch_scc0 .LBB0_2382
	global_load_dword v18, v17, s[6:7] sc1
	s_waitcnt vmcnt(0)
	v_cmp_eq_u32_e32 vcc, 0, v18
	s_cbranch_vccnz .LBB0_2384
	s_mov_b64 s[50:51], 0

.LBB0_2396:
	s_and_b32 s26, s30, 0xff
	s_mov_b64 s[24:25], -1
	s_cmp_lg_u32 s26, 0
	s_mov_b64 s[28:29], -1
	s_sleep 6
	s_cbranch_scc1 .LBB0_2399
	global_load_dword v3, v1, s[12:13] sc1
	s_waitcnt vmcnt(0)
	v_cmp_eq_u32_e32 vcc, 0, v3
	s_cbranch_vccnz .LBB0_2401
	s_mov_b64 s[28:29], 0
	s_mov_b64 s[26:27], -1

.LBB0_2413:
	s_and_b32 s24, s30, 0xff
	s_cmp_lg_u32 s24, 0
	s_mov_b64 s[26:27], -1
	s_sleep 6
	s_cbranch_scc1 .LBB0_2416
	global_load_dword v2, v1, s[12:13] sc1
	s_waitcnt vmcnt(0)
	v_cmp_eq_u32_e32 vcc, 0, v2
	s_cbranch_vccnz .LBB0_2418
	s_mov_b64 s[26:27], 0
	s_mov_b64 s[24:25], -1

.LBB0_2453:
	global_load_dword v15, v16, s[6:7] sc1
	global_load_dword v0, v16, s[8:9] sc1
	global_load_dword v1, v16, s[10:11] sc1
	global_load_dword v2, v16, s[12:13] sc1
	global_load_dword v3, v16, s[16:17] sc1
	global_load_dword v4, v16, s[18:19] sc1
	global_load_dword v5, v16, s[22:23] sc1
	global_load_dword v6, v16, s[24:25] sc1
	global_load_dword v7, v16, s[26:27] sc1
	global_load_dword v8, v16, s[28:29] sc1
	global_load_dword v9, v16, s[30:31] sc1
	global_load_dword v10, v16, s[34:35] sc1
	global_load_dword v11, v16, s[36:37] sc1
	global_load_dword v12, v16, s[38:39] sc1
	global_load_dword v13, v16, s[40:41] sc1
	global_load_dword v14, v16, s[42:43] sc1
	s_mov_b64 s[44:45], -1
	s_mov_b64 s[46:47], -1
	s_waitcnt vmcnt(14)
	v_add_u32_e32 v17, v0, v15
	s_waitcnt vmcnt(13)
	v_add_u32_e32 v17, v17, v1
	s_waitcnt vmcnt(12)
	v_add_u32_e32 v17, v17, v2
	s_waitcnt vmcnt(11)
	v_add_u32_e32 v17, v17, v3
	s_waitcnt vmcnt(10)
	v_add_u32_e32 v17, v17, v4
	s_waitcnt vmcnt(9)
	v_add_u32_e32 v17, v17, v5
	s_waitcnt vmcnt(8)
	v_add_u32_e32 v17, v17, v6
	s_waitcnt vmcnt(7)
	v_add_u32_e32 v17, v17, v7
	s_waitcnt vmcnt(6)
	v_add_u32_e32 v17, v17, v8
	s_waitcnt vmcnt(5)
	v_add_u32_e32 v17, v17, v9
	s_waitcnt vmcnt(4)
	v_add_u32_e32 v17, v17, v10
	s_waitcnt vmcnt(3)
	v_add_u32_e32 v17, v17, v11
	s_waitcnt vmcnt(2)
	v_add_u32_e32 v17, v17, v12
	s_waitcnt vmcnt(1)
	v_add_u32_e32 v17, v17, v13
	s_waitcnt vmcnt(0)
	v_add_u32_e32 v17, v17, v14
	v_cmp_eq_u32_e32 vcc, s33, v17
	s_cbranch_vccnz .LBB0_2452
	s_and_b32 s44, s50, 0xff
	s_cmp_eq_u32 s44, 0
	s_mov_b64 s[44:45], -1
	s_mov_b64 s[48:49], -1
	s_sleep 6
	s_cbranch_scc0 .LBB0_2457
	global_load_dword v17, v16, s[4:5] sc1
	s_waitcnt vmcnt(0)
	v_cmp_eq_u32_e32 vcc, 0, v17
	s_cbranch_vccnz .LBB0_2459
	s_mov_b64 s[48:49], 0

.LBB0_2471:
	s_and_b32 s24, s28, 0xff
	s_mov_b64 s[22:23], -1
	s_cmp_lg_u32 s24, 0
	s_mov_b64 s[26:27], -1
	s_sleep 6
	s_cbranch_scc1 .LBB0_2474
	global_load_dword v2, v0, s[10:11] sc1
	s_waitcnt vmcnt(0)
	v_cmp_eq_u32_e32 vcc, 0, v2
	s_cbranch_vccnz .LBB0_2476
	s_mov_b64 s[26:27], 0
	s_mov_b64 s[24:25], -1

.LBB0_2488:
	s_and_b32 s22, s28, 0xff
	s_cmp_lg_u32 s22, 0
	s_mov_b64 s[24:25], -1
	s_sleep 6
	s_cbranch_scc1 .LBB0_2491
	global_load_dword v1, v0, s[10:11] sc1
	s_waitcnt vmcnt(0)
	v_cmp_eq_u32_e32 vcc, 0, v1
	s_cbranch_vccnz .LBB0_2493
	s_mov_b64 s[24:25], 0
	s_mov_b64 s[22:23], -1
